# counted lgkmcnt in the MLP-up epilogue: the 7 waits in front of the piece stores allow the next piece's two LDS writes to stay outstanding (lgkmcnt(2)); otherwise the final e1 code
# speedup vs baseline: 1.0012x; 1.0012x over previous
.LBB0_655:
	s_lshl_b32 s11, s35, 8
	v_readlane_b32 s20, v252, 19
	s_cmp_lt_i32 s35, 32
	v_readlane_b32 s21, v252, 20
	s_cselect_b32 s18, s51, s21
	v_lshl_add_u32 v152, s34, 8, v143
	v_mov_b32_e32 v151, s18
	v_ashrrev_i32_e32 v153, 31, v152
	s_cselect_b32 s18, 13, 11
	v_lshlrev_b64 v[152:153], s18, v[152:153]
	s_mov_b32 s18, 0x60000
	s_cselect_b32 vcc_lo, s18, 0x18000
	s_mov_b32 s18, 0xc0000
	s_cselect_b32 s70, s18, 0x30000
	s_mov_b32 s18, 0xe0000
	s_cselect_b32 s58, s18, 0x38000
	s_mov_b32 s18, 0x220000
	s_cselect_b32 s56, s18, 0x88000
	s_mov_b32 s18, 0x240000
	s_cselect_b32 s46, s18, 0x90000
	s_mov_b32 s18, 0x260000
	s_cselect_b32 s36, s18, 0x98000
	s_mov_b32 s18, 0x280000
	s_cselect_b32 s34, s18, 0xa0000
	s_mov_b32 s18, 0x2a0000
	s_cselect_b32 s30, s18, 0xa8000
	s_mov_b32 s18, 0x2c0000
	v_cvt_pk_bf16_f32 v124, v124, v125
	v_cvt_pk_bf16_f32 v125, v126, v127
	v_cvt_pk_bf16_f32 v126, v120, v121
	v_cvt_pk_bf16_f32 v127, v122, v123
	v_cvt_pk_bf16_f32 v108, v108, v109
	v_cvt_pk_bf16_f32 v109, v110, v111
	v_cvt_pk_bf16_f32 v110, v104, v105
	v_cvt_pk_bf16_f32 v111, v106, v107
	s_cselect_b32 s13, 0, 0xffffe000
	s_cselect_b32 s19, s50, s20
	s_cselect_b32 s20, s18, 0xb0000
	s_mov_b32 s18, 0x2e0000
	ds_write_b128 v141, v[124:127]
	ds_write_b128 v147, v[108:111]
	v_mov_b32_e32 v150, s19
	s_cselect_b32 s19, s93, 0x800
	s_cselect_b32 s72, s85, 0x28000
	s_cselect_b32 s18, s18, 0xb8000
	s_add_i32 s96, s13, s11
	ds_read_b128 v[104:107], v148 offset:1024
	ds_read_b128 v[108:111], v142
	v_lshl_add_u64 v[150:151], v[152:153], 1, v[150:151]
	s_ashr_i32 s97, s96, 31
	v_lshl_add_u64 v[150:151], s[96:97], 1, v[150:151]
	v_lshl_add_u64 v[150:151], v[150:151], 0, s[80:81]
	v_lshl_add_u64 v[150:151], v[150:151], 0, v[160:161]
	s_lshl_b32 s96, s19, 4
	s_mov_b32 s97, s81
	v_cvt_pk_bf16_f32 v116, v116, v117
	v_cvt_pk_bf16_f32 v117, v118, v119
	v_cvt_pk_bf16_f32 v118, v112, v113
	v_cvt_pk_bf16_f32 v119, v114, v115
	v_cvt_pk_bf16_f32 v92, v92, v93
	v_cvt_pk_bf16_f32 v93, v94, v95
	v_cvt_pk_bf16_f32 v94, v88, v89
	v_cvt_pk_bf16_f32 v95, v90, v91
	s_waitcnt lgkmcnt(0)
	global_store_dwordx4 v[150:151], v[108:111], off nt
	ds_write_b128 v141, v[116:119]
	ds_write_b128 v147, v[92:95]
	v_lshl_add_u64 v[108:109], v[150:151], 0, s[96:97]
	global_store_dwordx4 v[108:109], v[104:107], off nt
	ds_read_b128 v[88:91], v142
	ds_read_b128 v[92:95], v148 offset:1024
	s_mov_b32 vcc_hi, s81
	v_cvt_pk_bf16_f32 v100, v100, v101
	v_cvt_pk_bf16_f32 v101, v102, v103
	v_cvt_pk_bf16_f32 v102, v96, v97
	v_cvt_pk_bf16_f32 v103, v98, v99
	v_cvt_pk_bf16_f32 v76, v76, v77
	v_cvt_pk_bf16_f32 v77, v78, v79
	v_cvt_pk_bf16_f32 v78, v72, v73
	v_cvt_pk_bf16_f32 v79, v74, v75
	v_lshl_add_u64 v[96:97], v[108:109], 0, s[96:97]
	v_lshl_add_u64 v[72:73], v[150:151], 0, vcc
	ds_write_b128 v141, v[100:103]
	ds_write_b128 v147, v[76:79]
	s_waitcnt lgkmcnt(0)
	global_store_dwordx4 v[96:97], v[88:91], off nt
	global_store_dwordx4 v[72:73], v[92:95], off nt
	ds_read_b128 v[72:75], v142
	ds_read_b128 v[76:79], v148 offset:1024
	s_lshl_b32 s96, s19, 5
	s_mov_b32 s73, s81
	v_cvt_pk_bf16_f32 v84, v84, v85
	v_cvt_pk_bf16_f32 v85, v86, v87
	v_cvt_pk_bf16_f32 v86, v80, v81
	v_cvt_pk_bf16_f32 v87, v82, v83
	v_cvt_pk_bf16_f32 v68, v68, v69
	v_cvt_pk_bf16_f32 v69, v70, v71
	v_cvt_pk_bf16_f32 v70, v64, v65
	v_cvt_pk_bf16_f32 v71, v66, v67
	v_lshl_add_u64 v[80:81], v[96:97], 0, s[96:97]
	v_lshl_add_u64 v[64:65], v[150:151], 0, s[72:73]
	ds_write_b128 v141, v[84:87]
	ds_write_b128 v147, v[68:71]
	s_waitcnt lgkmcnt(2)
	global_store_dwordx4 v[80:81], v[72:75], off nt
	global_store_dwordx4 v[64:65], v[76:79], off nt
	ds_read_b128 v[64:67], v142
	ds_read_b128 v[68:71], v148 offset:1024
	s_mov_b32 s71, s81
	v_cvt_pk_bf16_f32 v48, v48, v49
	v_cvt_pk_bf16_f32 v49, v50, v51
	v_cvt_pk_bf16_f32 v50, v40, v41
	v_lshl_add_u64 v[40:41], v[150:151], 0, s[70:71]
	s_mov_b32 s59, s81
	v_cvt_pk_bf16_f32 v60, v60, v61
	v_cvt_pk_bf16_f32 v61, v62, v63
	v_cvt_pk_bf16_f32 v62, v56, v57
	v_cvt_pk_bf16_f32 v63, v58, v59
	v_cvt_pk_bf16_f32 v51, v42, v43
	s_waitcnt lgkmcnt(0)
	global_store_dwordx4 v[40:41], v[64:67], off nt
	v_lshl_add_u64 v[40:41], v[150:151], 0, s[58:59]
	ds_write_b128 v141, v[60:63]
	ds_write_b128 v147, v[48:51]
	global_store_dwordx4 v[40:41], v[68:71], off nt
	ds_read_b128 v[40:43], v142
	ds_read_b128 v[48:51], v148 offset:1024
	s_mul_i32 s58, s19, 0xc0
	v_cvt_pk_bf16_f32 v32, v32, v33
	v_cvt_pk_bf16_f32 v33, v34, v35
	v_cvt_pk_bf16_f32 v34, v24, v25
	v_lshl_add_u64 v[24:25], v[80:81], 0, s[58:59]
	s_mov_b32 s57, s81
	v_cvt_pk_bf16_f32 v52, v52, v53
	v_cvt_pk_bf16_f32 v53, v54, v55
	v_cvt_pk_bf16_f32 v54, v44, v45
	v_cvt_pk_bf16_f32 v55, v46, v47
	v_cvt_pk_bf16_f32 v35, v26, v27
	s_waitcnt lgkmcnt(0)
	global_store_dwordx4 v[24:25], v[40:43], off nt
	v_lshl_add_u64 v[24:25], v[150:151], 0, s[56:57]
	ds_write_b128 v141, v[52:55]
	ds_write_b128 v147, v[32:35]
	global_store_dwordx4 v[24:25], v[48:51], off nt
	ds_read_b128 v[24:27], v142
	ds_read_b128 v[32:35], v148 offset:1024
	s_mov_b32 s47, s81
	v_cvt_pk_bf16_f32 v16, v16, v17
	v_cvt_pk_bf16_f32 v17, v18, v19
	v_cvt_pk_bf16_f32 v18, v8, v9
	v_lshl_add_u64 v[8:9], v[150:151], 0, s[46:47]
	s_mov_b32 s37, s81
	v_cvt_pk_bf16_f32 v36, v36, v37
	v_cvt_pk_bf16_f32 v37, v38, v39
	v_cvt_pk_bf16_f32 v38, v28, v29
	v_cvt_pk_bf16_f32 v39, v30, v31
	v_cvt_pk_bf16_f32 v19, v10, v11
	s_waitcnt lgkmcnt(0)
	global_store_dwordx4 v[8:9], v[24:27], off nt
	v_lshl_add_u64 v[8:9], v[150:151], 0, s[36:37]
	ds_write_b128 v141, v[36:39]
	ds_write_b128 v147, v[16:19]
	global_store_dwordx4 v[8:9], v[32:35], off nt
	ds_read_b128 v[8:11], v142
	ds_read_b128 v[16:19], v148 offset:1024
	v_cvt_pk_bf16_f32 v20, v20, v21
	v_cvt_pk_bf16_f32 v21, v22, v23
	v_cvt_pk_bf16_f32 v22, v12, v13
	v_cvt_pk_bf16_f32 v23, v14, v15
	v_cvt_pk_bf16_f32 v4, v4, v5
	v_cvt_pk_bf16_f32 v5, v6, v7
	v_cvt_pk_bf16_f32 v6, v0, v1
	v_cvt_pk_bf16_f32 v7, v2, v3
	s_mov_b32 s35, s81
	ds_write_b128 v141, v[20:23]
	ds_write_b128 v147, v[4:7]
	v_lshl_add_u64 v[0:1], v[150:151], 0, s[34:35]
	s_mov_b32 s31, s81
	s_waitcnt lgkmcnt(0)
	global_store_dwordx4 v[0:1], v[8:11], off nt
	v_lshl_add_u64 v[4:5], v[150:151], 0, s[30:31]
	ds_read_b128 v[0:3], v142
	global_store_dwordx4 v[4:5], v[16:19], off nt
	ds_read_b128 v[4:7], v148 offset:1024
	s_mov_b32 s21, s81
	v_lshl_add_u64 v[8:9], v[150:151], 0, s[20:21]
	s_mov_b32 s19, s81
	s_waitcnt lgkmcnt(0)
	global_store_dwordx4 v[8:9], v[0:3], off nt
	s_andn2_b64 vcc, exec, s[6:7]
	s_mov_b64 s[6:7], -1
	v_lshl_add_u64 v[0:1], v[150:151], 0, s[18:19]
	global_store_dwordx4 v[0:1], v[4:7], off nt
	s_cbranch_vccnz .LBB0_648
	s_andn2_b64 vcc, exec, s[4:5]
	s_cbranch_vccnz .LBB0_647
	s_barrier
	s_branch .LBB0_647

.LBB0_1043:
	v_max_i32_e32 v120, 0, v120
	v_max_i32_e32 v121, 0, v121
	v_max_i32_e32 v122, 0, v122
	v_max_i32_e32 v124, 0, v124
	v_mul_f32_e32 v151, v120, v120
	v_max_i32_e32 v120, 0, v125
	v_mul_f32_e32 v125, v121, v121
	v_max_i32_e32 v121, 0, v126
	v_mul_f32_e32 v126, v122, v122
	v_max_i32_e32 v122, 0, v127
	v_max_i32_e32 v123, 0, v123
	v_mul_f32_e32 v124, v124, v124
	v_mul_f32_e32 v120, v120, v120
	v_mul_f32_e32 v121, v121, v121
	v_mul_f32_e32 v122, v122, v122
	v_mul_f32_e32 v123, v123, v123
	v_cvt_pk_bf16_f32 v120, v124, v120
	v_cvt_pk_bf16_f32 v121, v121, v122
	v_cvt_pk_bf16_f32 v122, v151, v125
	v_cvt_pk_bf16_f32 v123, v126, v123
	v_max_i32_e32 v108, 0, v108
	v_max_i32_e32 v109, 0, v109
	v_max_i32_e32 v110, 0, v110
	ds_write_b128 v143, v[120:123]
	v_mul_f32_e32 v120, v108, v108
	v_max_i32_e32 v108, 0, v117
	v_mul_f32_e32 v117, v109, v109
	v_max_i32_e32 v109, 0, v118
	v_mul_f32_e32 v118, v110, v110
	v_max_i32_e32 v110, 0, v119
	v_lshl_add_u32 v140, s73, 8, v145
	v_max_i32_e32 v116, 0, v116
	v_mul_f32_e32 v109, v109, v109
	v_max_i32_e32 v111, 0, v111
	v_mul_f32_e32 v110, v110, v110
	v_max_i32_e32 v104, 0, v104
	v_max_i32_e32 v105, 0, v105
	v_max_i32_e32 v106, 0, v106
	v_ashrrev_i32_e32 v141, 31, v140
	v_mul_f32_e32 v116, v116, v116
	v_mul_f32_e32 v108, v108, v108
	v_mul_f32_e32 v111, v111, v111
	v_cvt_pk_bf16_f32 v109, v109, v110
	v_cvt_pk_bf16_f32 v110, v120, v117
	v_max_i32_e32 v112, 0, v112
	v_mul_f32_e32 v120, v104, v104
	v_max_i32_e32 v104, 0, v113
	v_mul_f32_e32 v113, v105, v105
	v_max_i32_e32 v105, 0, v114
	v_mul_f32_e32 v114, v106, v106
	v_max_i32_e32 v106, 0, v115
	v_max_i32_e32 v107, 0, v107
	s_lshl_b32 s30, s72, 8
	v_lshlrev_b64 v[140:141], 14, v[140:141]
	v_cvt_pk_bf16_f32 v108, v116, v108
	v_cvt_pk_bf16_f32 v111, v118, v111
	v_mul_f32_e32 v112, v112, v112
	v_mul_f32_e32 v104, v104, v104
	v_mul_f32_e32 v105, v105, v105
	v_mul_f32_e32 v106, v106, v106
	v_mul_f32_e32 v107, v107, v107
	v_lshl_add_u64 v[140:141], s[50:51], 0, v[140:141]
	s_ashr_i32 s31, s30, 31
	ds_write_b128 v149, v[108:111]
	v_cvt_pk_bf16_f32 v104, v112, v104
	v_cvt_pk_bf16_f32 v105, v105, v106
	v_cvt_pk_bf16_f32 v106, v120, v113
	v_cvt_pk_bf16_f32 v107, v114, v107
	v_max_i32_e32 v96, 0, v96
	v_max_i32_e32 v97, 0, v97
	v_max_i32_e32 v98, 0, v98
	v_lshl_add_u64 v[140:141], s[30:31], 1, v[140:141]
	ds_read_b128 v[108:111], v150 offset:1024
	ds_read_b128 v[116:119], v144
	ds_write_b128 v143, v[104:107]
	v_max_i32_e32 v100, 0, v100
	v_mul_f32_e32 v104, v96, v96
	v_max_i32_e32 v96, 0, v101
	v_mul_f32_e32 v101, v97, v97
	v_max_i32_e32 v97, 0, v102
	v_mul_f32_e32 v102, v98, v98
	v_max_i32_e32 v98, 0, v103
	v_max_i32_e32 v99, 0, v99
	v_lshl_add_u64 v[140:141], v[140:141], 0, s[80:81]
	v_mul_f32_e32 v100, v100, v100
	v_mul_f32_e32 v96, v96, v96
	v_mul_f32_e32 v97, v97, v97
	v_mul_f32_e32 v98, v98, v98
	v_mul_f32_e32 v99, v99, v99
	v_lshl_add_u64 v[140:141], v[140:141], 0, v[160:161]
	v_cvt_pk_bf16_f32 v96, v100, v96
	v_cvt_pk_bf16_f32 v97, v97, v98
	v_cvt_pk_bf16_f32 v98, v104, v101
	v_cvt_pk_bf16_f32 v99, v102, v99
	v_max_i32_e32 v88, 0, v88
	v_max_i32_e32 v89, 0, v89
	v_max_i32_e32 v90, 0, v90
	ds_write_b128 v149, v[96:99]
	v_add_co_u32_e32 v96, vcc, s92, v140
	v_max_i32_e32 v92, 0, v92
	v_mul_f32_e32 v104, v88, v88
	v_max_i32_e32 v88, 0, v93
	v_mul_f32_e32 v93, v89, v89
	v_max_i32_e32 v89, 0, v94
	v_mul_f32_e32 v94, v90, v90
	v_max_i32_e32 v90, 0, v95
	v_max_i32_e32 v91, 0, v91
	v_addc_co_u32_e32 v97, vcc, 0, v141, vcc
	v_mul_f32_e32 v92, v92, v92
	v_mul_f32_e32 v88, v88, v88
	v_mul_f32_e32 v89, v89, v89
	v_mul_f32_e32 v90, v90, v90
	v_mul_f32_e32 v91, v91, v91
	s_waitcnt lgkmcnt(0)
	global_store_dwordx4 v[140:141], v[116:119], off nt
	global_store_dwordx4 v[96:97], v[108:111], off nt
	v_cvt_pk_bf16_f32 v88, v92, v88
	v_cvt_pk_bf16_f32 v89, v89, v90
	v_cvt_pk_bf16_f32 v90, v104, v93
	v_cvt_pk_bf16_f32 v91, v94, v91
	v_max_i32_e32 v80, 0, v80
	v_max_i32_e32 v81, 0, v81
	v_max_i32_e32 v82, 0, v82
	ds_read_b128 v[96:99], v144
	ds_read_b128 v[100:103], v150 offset:1024
	ds_write_b128 v143, v[88:91]
	v_max_i32_e32 v84, 0, v84
	v_mul_f32_e32 v88, v80, v80
	v_max_i32_e32 v80, 0, v85
	v_mul_f32_e32 v85, v81, v81
	v_max_i32_e32 v81, 0, v86
	v_mul_f32_e32 v86, v82, v82
	v_max_i32_e32 v82, 0, v87
	v_max_i32_e32 v83, 0, v83
	v_mul_f32_e32 v84, v84, v84
	v_mul_f32_e32 v80, v80, v80
	v_mul_f32_e32 v81, v81, v81
	v_mul_f32_e32 v82, v82, v82
	v_mul_f32_e32 v83, v83, v83
	v_cvt_pk_bf16_f32 v80, v84, v80
	v_cvt_pk_bf16_f32 v81, v81, v82
	v_cvt_pk_bf16_f32 v82, v88, v85
	v_cvt_pk_bf16_f32 v83, v86, v83
	s_mov_b32 s11, 0x40000
	ds_write_b128 v149, v[80:83]
	v_add_co_u32_e32 v80, vcc, s11, v140
	s_mov_b32 s11, 0x60000
	s_nop 0
	v_addc_co_u32_e32 v81, vcc, 0, v141, vcc
	v_max_i32_e32 v72, 0, v72
	v_max_i32_e32 v73, 0, v73
	v_max_i32_e32 v74, 0, v74
	s_waitcnt lgkmcnt(2)
	global_store_dwordx4 v[80:81], v[96:99], off nt
	v_add_co_u32_e32 v80, vcc, s11, v140
	v_max_i32_e32 v76, 0, v76
	v_mul_f32_e32 v88, v72, v72
	v_max_i32_e32 v72, 0, v77
	v_mul_f32_e32 v77, v73, v73
	v_max_i32_e32 v73, 0, v78
	v_mul_f32_e32 v78, v74, v74
	v_max_i32_e32 v74, 0, v79
	v_max_i32_e32 v75, 0, v75
	v_addc_co_u32_e32 v81, vcc, 0, v141, vcc
	v_mul_f32_e32 v76, v76, v76
	v_mul_f32_e32 v72, v72, v72
	v_mul_f32_e32 v73, v73, v73
	v_mul_f32_e32 v74, v74, v74
	v_mul_f32_e32 v75, v75, v75
	global_store_dwordx4 v[80:81], v[100:103], off nt
	v_cvt_pk_bf16_f32 v72, v76, v72
	v_cvt_pk_bf16_f32 v73, v73, v74
	v_cvt_pk_bf16_f32 v74, v88, v77
	v_cvt_pk_bf16_f32 v75, v78, v75
	v_max_i32_e32 v64, 0, v64
	v_max_i32_e32 v65, 0, v65
	v_max_i32_e32 v66, 0, v66
	ds_read_b128 v[80:83], v144
	ds_read_b128 v[84:87], v150 offset:1024
	ds_write_b128 v143, v[72:75]
	v_max_i32_e32 v68, 0, v68
	v_mul_f32_e32 v72, v64, v64
	v_max_i32_e32 v64, 0, v69
	v_mul_f32_e32 v69, v65, v65
	v_max_i32_e32 v65, 0, v70
	v_mul_f32_e32 v70, v66, v66
	v_max_i32_e32 v66, 0, v71
	v_max_i32_e32 v67, 0, v67
	v_mul_f32_e32 v68, v68, v68
	v_mul_f32_e32 v64, v64, v64
	v_mul_f32_e32 v65, v65, v65
	v_mul_f32_e32 v66, v66, v66
	v_mul_f32_e32 v67, v67, v67
	v_cvt_pk_bf16_f32 v64, v68, v64
	v_cvt_pk_bf16_f32 v65, v65, v66
	v_cvt_pk_bf16_f32 v66, v72, v69
	v_cvt_pk_bf16_f32 v67, v70, v67
	ds_write_b128 v149, v[64:67]
	v_add_co_u32_e32 v64, vcc, s61, v140
	v_max_i32_e32 v56, 0, v56
	s_nop 0
	v_addc_co_u32_e32 v65, vcc, 0, v141, vcc
	v_max_i32_e32 v57, 0, v57
	v_max_i32_e32 v58, 0, v58
	s_waitcnt lgkmcnt(2)
	global_store_dwordx4 v[64:65], v[80:83], off nt
	v_add_co_u32_e32 v64, vcc, s85, v140
	v_max_i32_e32 v60, 0, v60
	v_mul_f32_e32 v72, v56, v56
	v_max_i32_e32 v56, 0, v61
	v_mul_f32_e32 v61, v57, v57
	v_max_i32_e32 v57, 0, v62
	v_mul_f32_e32 v62, v58, v58
	v_max_i32_e32 v58, 0, v63
	v_max_i32_e32 v59, 0, v59
	v_addc_co_u32_e32 v65, vcc, 0, v141, vcc
	v_mul_f32_e32 v60, v60, v60
	v_mul_f32_e32 v56, v56, v56
	v_mul_f32_e32 v57, v57, v57
	v_mul_f32_e32 v58, v58, v58
	v_mul_f32_e32 v59, v59, v59
	global_store_dwordx4 v[64:65], v[84:87], off nt
	v_cvt_pk_bf16_f32 v56, v60, v56
	v_cvt_pk_bf16_f32 v57, v57, v58
	v_cvt_pk_bf16_f32 v58, v72, v61
	v_cvt_pk_bf16_f32 v59, v62, v59
	v_max_i32_e32 v48, 0, v48
	v_max_i32_e32 v49, 0, v49
	v_max_i32_e32 v50, 0, v50
	ds_read_b128 v[64:67], v144
	ds_read_b128 v[68:71], v150 offset:1024
	ds_write_b128 v143, v[56:59]
	v_max_i32_e32 v52, 0, v52
	v_mul_f32_e32 v56, v48, v48
	v_max_i32_e32 v48, 0, v53
	v_mul_f32_e32 v53, v49, v49
	v_max_i32_e32 v49, 0, v54
	v_mul_f32_e32 v54, v50, v50
	v_max_i32_e32 v50, 0, v55
	v_max_i32_e32 v51, 0, v51
	v_mul_f32_e32 v52, v52, v52
	v_mul_f32_e32 v48, v48, v48
	v_mul_f32_e32 v49, v49, v49
	v_mul_f32_e32 v50, v50, v50
	v_mul_f32_e32 v51, v51, v51
	v_cvt_pk_bf16_f32 v48, v52, v48
	v_cvt_pk_bf16_f32 v49, v49, v50
	v_cvt_pk_bf16_f32 v50, v56, v53
	v_cvt_pk_bf16_f32 v51, v54, v51
	s_mov_b32 s11, 0xc0000
	ds_write_b128 v149, v[48:51]
	v_add_co_u32_e32 v48, vcc, s11, v140
	s_mov_b32 s11, 0xe0000
	s_nop 0
	v_addc_co_u32_e32 v49, vcc, 0, v141, vcc
	v_max_i32_e32 v40, 0, v40
	v_max_i32_e32 v41, 0, v41
	v_max_i32_e32 v42, 0, v42
	s_waitcnt lgkmcnt(2)
	global_store_dwordx4 v[48:49], v[64:67], off nt
	v_add_co_u32_e32 v48, vcc, s11, v140
	v_max_i32_e32 v44, 0, v44
	v_mul_f32_e32 v56, v40, v40
	v_max_i32_e32 v40, 0, v45
	v_mul_f32_e32 v45, v41, v41
	v_max_i32_e32 v41, 0, v46
	v_mul_f32_e32 v46, v42, v42
	v_max_i32_e32 v42, 0, v47
	v_max_i32_e32 v43, 0, v43
	v_addc_co_u32_e32 v49, vcc, 0, v141, vcc
	v_mul_f32_e32 v44, v44, v44
	v_mul_f32_e32 v40, v40, v40
	v_mul_f32_e32 v41, v41, v41
	v_mul_f32_e32 v42, v42, v42
	v_mul_f32_e32 v43, v43, v43
	global_store_dwordx4 v[48:49], v[68:71], off nt
	v_cvt_pk_bf16_f32 v40, v44, v40
	v_cvt_pk_bf16_f32 v41, v41, v42
	v_cvt_pk_bf16_f32 v42, v56, v45
	v_cvt_pk_bf16_f32 v43, v46, v43
	v_max_i32_e32 v32, 0, v32
	v_max_i32_e32 v33, 0, v33
	v_max_i32_e32 v34, 0, v34
	ds_read_b128 v[48:51], v144
	ds_read_b128 v[52:55], v150 offset:1024
	ds_write_b128 v143, v[40:43]
	v_max_i32_e32 v36, 0, v36
	v_mul_f32_e32 v40, v32, v32
	v_max_i32_e32 v32, 0, v37
	v_mul_f32_e32 v37, v33, v33
	v_max_i32_e32 v33, 0, v38
	v_mul_f32_e32 v38, v34, v34
	v_max_i32_e32 v34, 0, v39
	v_max_i32_e32 v35, 0, v35
	v_mul_f32_e32 v36, v36, v36
	v_mul_f32_e32 v32, v32, v32
	v_mul_f32_e32 v33, v33, v33
	v_mul_f32_e32 v34, v34, v34
	v_mul_f32_e32 v35, v35, v35
	v_cvt_pk_bf16_f32 v32, v36, v32
	v_cvt_pk_bf16_f32 v33, v33, v34
	v_cvt_pk_bf16_f32 v34, v40, v37
	v_cvt_pk_bf16_f32 v35, v38, v35
	s_mov_b32 s11, 0x200000
	ds_write_b128 v149, v[32:35]
	v_add_co_u32_e32 v32, vcc, s11, v140
	s_mov_b32 s11, 0x220000
	s_nop 0
	v_addc_co_u32_e32 v33, vcc, 0, v141, vcc
	v_max_i32_e32 v24, 0, v24
	v_max_i32_e32 v25, 0, v25
	v_max_i32_e32 v26, 0, v26
	s_waitcnt lgkmcnt(2)
	global_store_dwordx4 v[32:33], v[48:51], off nt
	v_add_co_u32_e32 v32, vcc, s11, v140
	v_max_i32_e32 v28, 0, v28
	v_mul_f32_e32 v40, v24, v24
	v_max_i32_e32 v24, 0, v29
	v_mul_f32_e32 v29, v25, v25
	v_max_i32_e32 v25, 0, v30
	v_mul_f32_e32 v30, v26, v26
	v_max_i32_e32 v26, 0, v31
	v_max_i32_e32 v27, 0, v27
	v_addc_co_u32_e32 v33, vcc, 0, v141, vcc
	v_mul_f32_e32 v28, v28, v28
	v_mul_f32_e32 v24, v24, v24
	v_mul_f32_e32 v25, v25, v25
	v_mul_f32_e32 v26, v26, v26
	v_mul_f32_e32 v27, v27, v27
	global_store_dwordx4 v[32:33], v[52:55], off nt
	v_cvt_pk_bf16_f32 v24, v28, v24
	v_cvt_pk_bf16_f32 v25, v25, v26
	v_cvt_pk_bf16_f32 v26, v40, v29
	v_cvt_pk_bf16_f32 v27, v30, v27
	v_max_i32_e32 v16, 0, v16
	v_max_i32_e32 v17, 0, v17
	v_max_i32_e32 v18, 0, v18
	ds_read_b128 v[32:35], v144
	ds_read_b128 v[36:39], v150 offset:1024
	ds_write_b128 v143, v[24:27]
	v_max_i32_e32 v20, 0, v20
	v_mul_f32_e32 v24, v16, v16
	v_max_i32_e32 v16, 0, v21
	v_mul_f32_e32 v21, v17, v17
	v_max_i32_e32 v17, 0, v22
	v_mul_f32_e32 v22, v18, v18
	v_max_i32_e32 v18, 0, v23
	v_max_i32_e32 v19, 0, v19
	v_mul_f32_e32 v20, v20, v20
	v_mul_f32_e32 v16, v16, v16
	v_mul_f32_e32 v17, v17, v17
	v_mul_f32_e32 v18, v18, v18
	v_mul_f32_e32 v19, v19, v19
	v_cvt_pk_bf16_f32 v16, v20, v16
	v_cvt_pk_bf16_f32 v17, v17, v18
	v_cvt_pk_bf16_f32 v18, v24, v21
	v_cvt_pk_bf16_f32 v19, v22, v19
	s_mov_b32 s11, 0x240000
	ds_write_b128 v149, v[16:19]
	v_add_co_u32_e32 v16, vcc, s11, v140
	s_mov_b32 s11, 0x260000
	s_nop 0
	v_addc_co_u32_e32 v17, vcc, 0, v141, vcc
	v_max_i32_e32 v8, 0, v8
	v_max_i32_e32 v9, 0, v9
	v_max_i32_e32 v10, 0, v10
	s_waitcnt lgkmcnt(2)
	global_store_dwordx4 v[16:17], v[32:35], off nt
	v_add_co_u32_e32 v16, vcc, s11, v140
	v_max_i32_e32 v12, 0, v12
	v_mul_f32_e32 v24, v8, v8
	v_max_i32_e32 v8, 0, v13
	v_mul_f32_e32 v13, v9, v9
	v_max_i32_e32 v9, 0, v14
	v_mul_f32_e32 v14, v10, v10
	v_max_i32_e32 v10, 0, v15
	v_max_i32_e32 v11, 0, v11
	v_addc_co_u32_e32 v17, vcc, 0, v141, vcc
	v_mul_f32_e32 v12, v12, v12
	v_mul_f32_e32 v8, v8, v8
	v_mul_f32_e32 v9, v9, v9
	v_mul_f32_e32 v10, v10, v10
	v_mul_f32_e32 v11, v11, v11
	global_store_dwordx4 v[16:17], v[36:39], off nt
	v_cvt_pk_bf16_f32 v8, v12, v8
	v_cvt_pk_bf16_f32 v9, v9, v10
	v_cvt_pk_bf16_f32 v10, v24, v13
	v_cvt_pk_bf16_f32 v11, v14, v11
	v_max_i32_e32 v0, 0, v0
	v_max_i32_e32 v1, 0, v1
	v_max_i32_e32 v2, 0, v2
	ds_read_b128 v[16:19], v144
	ds_read_b128 v[20:23], v150 offset:1024
	ds_write_b128 v143, v[8:11]
	v_max_i32_e32 v4, 0, v4
	v_mul_f32_e32 v8, v0, v0
	v_max_i32_e32 v0, 0, v5
	v_mul_f32_e32 v5, v1, v1
	v_max_i32_e32 v1, 0, v6
	v_mul_f32_e32 v6, v2, v2
	v_max_i32_e32 v2, 0, v7
	v_max_i32_e32 v3, 0, v3
	v_mul_f32_e32 v4, v4, v4
	v_mul_f32_e32 v0, v0, v0
	v_mul_f32_e32 v1, v1, v1
	v_mul_f32_e32 v2, v2, v2
	v_mul_f32_e32 v3, v3, v3
	v_cvt_pk_bf16_f32 v0, v4, v0
	v_cvt_pk_bf16_f32 v1, v1, v2
	v_cvt_pk_bf16_f32 v2, v8, v5
	v_cvt_pk_bf16_f32 v3, v6, v3
	s_mov_b32 s11, 0x280000
	ds_write_b128 v149, v[0:3]
	v_add_co_u32_e32 v0, vcc, s11, v140
	s_mov_b32 s11, 0x2a0000
	s_nop 0
	v_addc_co_u32_e32 v1, vcc, 0, v141, vcc
	s_waitcnt lgkmcnt(2)
	global_store_dwordx4 v[0:1], v[16:19], off nt
	v_add_co_u32_e32 v0, vcc, s11, v140
	s_mov_b32 s90, 0x3fb8aa3b
	s_nop 0
	v_addc_co_u32_e32 v1, vcc, 0, v141, vcc
	global_store_dwordx4 v[0:1], v[20:23], off nt
	ds_read_b128 v[0:3], v144
	ds_read_b128 v[4:7], v150 offset:1024
	v_add_co_u32_e32 v8, vcc, 0x2c0000, v140
	s_nop 1
	v_addc_co_u32_e32 v9, vcc, 0, v141, vcc
	s_waitcnt lgkmcnt(0)
	global_store_dwordx4 v[8:9], v[0:3], off nt
	s_nop 1
	v_add_co_u32_e32 v0, vcc, 0x2e0000, v140
	s_nop 1
	v_addc_co_u32_e32 v1, vcc, 0, v141, vcc
	s_andn2_b64 vcc, exec, s[6:7]
	s_mov_b64 s[6:7], -1
	global_store_dwordx4 v[0:1], v[4:7], off nt
	s_cbranch_vccnz .LBB0_1032
	s_andn2_b64 vcc, exec, s[4:5]
	s_cbranch_vccnz .LBB0_1031
	s_barrier
	s_branch .LBB0_1031
